# code placement: 4-byte pads put the GU1 and WIN GEMM K-loops back at the baseline byte phase (96 of 128 MFMAs 8-byte aligned); other loops unchanged
# speedup vs baseline: 1.0024x; 1.0024x over previous
; #define PG8_WAIT_V(n) asm volatile("s_waitcnt vmcnt(" #n ")" ::: "memory")
; #define PG8_BAR __builtin_amdgcn_s_barrier()
; template <class Epi, class Sched, bool ALIGN_EPI = false, bool SP2 = false, bool FP8 = false, bool ABLK = false>
; __device__ __forceinline__ void gemm_phase(PG8_LAS unsigned char* lds, const Gemm g, const Sched& S, const Epi& E) {
;     ...
;     const int tid = tid_, wid = __builtin_amdgcn_readfirstlane(tid >> 6), lane = tid & 63, wr = wid >> 2, wc = wid & 3, fr = lane & 15, fq = lane >> 4;
;     const int K = g.K, nt = K / BK;
;     unsigned voffA[2], voffB[2];
; #pragma unroll
;     for (int i = 0; i < 2; ++i) { int R, C; stage_rc(tid * 16 + i * 8192, R, C); const int Rb = Epi::PERM ? ((R & ~31) + perm32(R & 31)) : R;
;         voffA[i] = ABLK ? (unsigned)(((((R >> 6) * 4 + (C >> 4)) * 8 + ((R >> 4) & 3)) * 64 + ((C >> 3) & 1) * 32 + (R & 15) * 2) * 8) : (unsigned)(R * K + C) * 2u; voffB[i] = (unsigned)(Rb * K + C) * 2u; }
;     const size_t kstep = (size_t)(BK * 2);
;     const size_t hstep = (size_t)HALF * K * 2;
;     const size_t kstepA = ABLK ? (size_t)32768 : kstep, hstepA = ABLK ? (size_t)2048 : hstep;
;     const size_t tstep = 2 * hstep;
;     const unsigned ldsw = (unsigned)wid * 1024u;
;     const int aoff = lds_byte(wr * 64 + fr, fq * 8), boff = lds_byte(wc * 32 + fr, fq * 8);
;     ...
;     Unit cur, nxt; int ui = 0;
;     if (!S.next(0, cur)) return;
;     f32x4 acc[2][2][4][2];
; #pragma unroll
;     for (int a = 0; a < 2; ++a)
; #pragma unroll
;         for (int b = 0; b < 2; ++b)
; #pragma unroll
;             for (int m = 0; m < 4; ++m)
; #pragma unroll
;                 for (int n = 0; n < 2; ++n) acc[a][b][m][n] = (f32x4){0.f, 0.f, 0.f, 0.f};
;     bf16x8 At[4][2], B0[2][2], B1[2][2];
;     const char* cA = (const char*)g.A + (size_t)cur.pm * tstep; const char* cB = (const char*)g.Bt + (size_t)cur.pn * tstep;
;     S.a_ready(cur);
;     if constexpr (SP2) {
;         PG8_STAGE(PG8_SB(0, 0), cB, voffB); PG8_STAGE(PG8_SB(0, 1), cB + hstep, voffB); PG8_STAGE(PG8_SA(0, 0), cA, voffA); PG8_STAGE(PG8_SA(0, 1), cA + hstepA, voffA);
;         if (wr == 1) PG8_BAR;
;         PG8_WAIT_V(2); PG8_BAR;
;         PG8_STAGE(PG8_SB(1, 0), cB + kstep, voffB); PG8_STAGE(PG8_SA(1, 0), cA + kstepA, voffA); PG8_STAGE(PG8_SB(1, 1), cB + hstep + kstep, voffB);
;         PG8_WAIT_V(0); PG8_BAR;
;     } else {
.LBB0_421:
	s_andn2_b64 vcc, exec, s[4:5]
	s_cbranch_vccnz .LBB0_488
	v_readlane_b32 s6, v253, 23
	v_mov_b32_e32 v1, v0
	s_mov_b64 s[4:5], s[66:67]
	s_nop 0
	v_mov_b32_e32 v12, v0
	v_readlane_b32 s7, v253, 24
	s_andn2_b64 vcc, exec, s[6:7]
	v_readfirstlane_b32 s50, v12
	s_cbranch_vccnz .LBB0_438
	v_lshlrev_b32_e32 v1, 4, v12
	v_add_u32_e32 v2, 0x2000, v1
	v_ashrrev_i32_e32 v4, 31, v2
	v_lshrrev_b32_e32 v4, 22, v4
	v_add_u32_e32 v4, v2, v4
	v_ashrrev_i32_e32 v13, 10, v4
	v_mul_i32_i24_e32 v4, 0x400, v13
	v_sub_u32_e32 v2, v2, v4
	v_lshrrev_b32_e32 v4, 4, v2
	v_bitop3_b32 v2, v4, v2, 32 bitop3:0x6c
	v_ashrrev_i32_e32 v4, 31, v2
	v_lshrrev_b32_e32 v4, 26, v4
	v_add_u32_e32 v4, v2, v4
	s_waitcnt lgkmcnt(0)
	v_lshlrev_b32_e32 v5, 3, v13
	v_ashrrev_i32_e32 v14, 6, v4
	v_and_b32_e32 v5, -16, v5
	v_add_u32_e32 v5, v14, v5
	v_and_b32_e32 v6, 3, v14
	s_mov_b32 s18, 0x1fffe0
	v_lshrrev_b32_e32 v7, 2, v5
	v_lshlrev_b32_e32 v8, 1, v5
	v_and_b32_e32 v4, 0xc0, v4
	v_and_or_b32 v6, v5, s18, v6
	v_and_b32_e32 v7, 4, v7
	v_and_b32_e32 v8, 24, v8
	v_sub_u32_e32 v2, v2, v4
	v_or3_b32 v6, v6, v7, v8
	v_lshlrev_b32_e32 v7, 5, v13
	v_ashrrev_i16_sdwa v2, v244, sext(v2) dst_sel:DWORD dst_unused:UNUSED_PAD src0_sel:DWORD src1_sel:BYTE_0
	v_and_b32_e32 v7, 32, v7
	v_bfe_i32 v15, v2, 0, 16
	v_add_lshl_u32 v2, v7, v15, 1
	s_waitcnt vmcnt(0)
	v_lshl_add_u32 v152, v6, 11, v2
	v_lshl_add_u32 v154, v5, 11, v2
	v_bfe_i32 v2, v12, 27, 1
	v_lshrrev_b32_e32 v2, 22, v2
	v_add_u32_e32 v2, v1, v2
	s_load_dwordx2 s[38:39], s[4:5], 0xd0
	v_and_b32_e32 v2, 0xfffffc00, v2
	v_sub_u32_e32 v1, v1, v2
	v_lshrrev_b32_e32 v2, 4, v1
	v_ashrrev_i32_e32 v4, 31, v12
	v_readlane_b32 s4, v252, 18
	v_bitop3_b32 v1, v2, v1, 32 bitop3:0x6c
	v_lshrrev_b32_e32 v4, 26, v4
	s_mul_i32 s4, s4, 0x2d80000
	v_ashrrev_i32_e32 v2, 31, v1
	v_add_u32_e32 v4, v12, v4
	v_readlane_b32 s5, v252, 19
	s_waitcnt lgkmcnt(0)
	s_add_u32 s4, s38, s4
	v_lshrrev_b32_e32 v2, 26, v2
	v_ashrrev_i32_e32 v17, 6, v4
	s_addc_u32 s5, s39, 0
	v_add_u32_e32 v2, v1, v2
	v_lshlrev_b32_e32 v4, 3, v17
	s_add_u32 s6, s4, 0x1e00000
	v_ashrrev_i32_e32 v16, 6, v2
	v_and_b32_e32 v4, -16, v4
	s_addc_u32 s7, s5, 0
	v_add_u32_e32 v4, v16, v4
	s_add_u32 s8, s38, 0x7a00000
	v_and_b32_e32 v5, 3, v16
	v_lshrrev_b32_e32 v6, 2, v4
	v_lshlrev_b32_e32 v7, 1, v4
	v_and_b32_e32 v2, 0xc0, v2
	s_addc_u32 s9, s39, 0
	s_ashr_i32 s5, s50, 6
	v_and_or_b32 v5, v4, s18, v5
	v_and_b32_e32 v6, 4, v6
	v_and_b32_e32 v7, 24, v7
	v_sub_u32_e32 v1, v1, v2
	s_ashr_i32 s4, s50, 8
	s_lshl_b32 s17, s5, 10
	v_or3_b32 v5, v5, v6, v7
	v_lshlrev_b32_e32 v6, 5, v17
	v_ashrrev_i16_sdwa v1, v244, sext(v1) dst_sel:DWORD dst_unused:UNUSED_PAD src0_sel:DWORD src1_sel:BYTE_0
	v_readlane_b32 s18, v254, 37
	v_and_b32_e32 v6, 32, v6
	v_bfe_i32 v18, v1, 0, 16
	v_readlane_b32 s19, v254, 38
	s_add_u32 s62, s6, s18
	v_add_lshl_u32 v1, v6, v18, 1
	s_addc_u32 s63, s7, s19
	s_add_i32 s18, s17, 0
	v_lshl_add_u32 v2, v5, 11, v1
	s_add_i32 m0, s18, 0x10000
	v_lshl_add_u32 v156, v4, 11, v1
	global_load_lds_dwordx4 v2, s[62:63]
	s_add_i32 m0, s18, 0x12000
	s_add_u32 s20, s62, 0x40000
	global_load_lds_dwordx4 v152, s[62:63]
	s_addc_u32 s21, s63, 0
	s_add_i32 m0, s18, 0x14000
	v_mov_b32_e32 v153, v3
	global_load_lds_dwordx4 v2, s[20:21]
	s_add_i32 m0, s18, 0x16000
	v_mov_b32_e32 v157, v3
	global_load_lds_dwordx4 v152, s[20:21]
	v_readlane_b32 s20, v254, 35
	v_readlane_b32 s21, v254, 36
	s_add_u32 s60, s8, s20
	s_addc_u32 s61, s9, s21
	s_add_i32 s19, s18, 0x2000
	s_mov_b32 m0, s18
	s_add_u32 s22, s60, 0x40000
	global_load_lds_dwordx4 v156, s[60:61]
	s_mov_b32 m0, s19
	s_addc_u32 s23, s61, 0
	s_add_i32 s20, s18, 0x4000
	global_load_lds_dwordx4 v154, s[60:61]
	s_mov_b32 m0, s20
	s_add_i32 s21, s18, 0x6000
	global_load_lds_dwordx4 v156, s[22:23]
	s_mov_b32 m0, s21
	v_mov_b32_e32 v155, v3
	global_load_lds_dwordx4 v154, s[22:23]
	s_cmp_eq_u32 s4, 1
	v_lshl_add_u64 v[10:11], s[62:63], 0, v[2:3]
	v_lshl_add_u64 v[8:9], s[62:63], 0, v[152:153]
	v_lshl_add_u64 v[4:5], s[60:61], 0, v[156:157]
	s_cselect_b64 s[44:45], -1, 0
	s_cmp_lg_u32 s4, 1
	v_lshl_add_u64 v[6:7], s[60:61], 0, v[154:155]
	s_cbranch_scc1 .LBB0_425
	s_barrier

; #define PG8_WAIT_V(n) asm volatile("s_waitcnt vmcnt(" #n ")" ::: "memory")
; #define PG8_BAR __builtin_amdgcn_s_barrier()
; template <class Epi, class Sched, bool ALIGN_EPI = false, bool SP2 = false, bool FP8 = false, bool ABLK = false>
; __device__ __forceinline__ void gemm_phase(PG8_LAS unsigned char* lds, const Gemm g, const Sched& S, const Epi& E) {
;     ...
;     const int tid = tid_, wid = __builtin_amdgcn_readfirstlane(tid >> 6), lane = tid & 63, wr = wid >> 2, wc = wid & 3, fr = lane & 15, fq = lane >> 4;
;     const int K = g.K, nt = K / BK;
;     unsigned voffA[2], voffB[2];
; #pragma unroll
;     for (int i = 0; i < 2; ++i) { int R, C; stage_rc(tid * 16 + i * 8192, R, C); const int Rb = Epi::PERM ? ((R & ~31) + perm32(R & 31)) : R;
;         voffA[i] = ABLK ? (unsigned)(((((R >> 6) * 4 + (C >> 4)) * 8 + ((R >> 4) & 3)) * 64 + ((C >> 3) & 1) * 32 + (R & 15) * 2) * 8) : (unsigned)(R * K + C) * 2u; voffB[i] = (unsigned)(Rb * K + C) * 2u; }
;     const size_t kstep = (size_t)(BK * 2);
;     const size_t hstep = (size_t)HALF * K * 2;
;     const size_t kstepA = ABLK ? (size_t)32768 : kstep, hstepA = ABLK ? (size_t)2048 : hstep;
;     const size_t tstep = 2 * hstep;
;     const unsigned ldsw = (unsigned)wid * 1024u;
;     const int aoff = lds_byte(wr * 64 + fr, fq * 8), boff = lds_byte(wc * 32 + fr, fq * 8);
;     ...
;     Unit cur, nxt; int ui = 0;
;     if (!S.next(0, cur)) return;
;     f32x4 acc[2][2][4][2];
; #pragma unroll
;     for (int a = 0; a < 2; ++a)
; #pragma unroll
;         for (int b = 0; b < 2; ++b)
; #pragma unroll
;             for (int m = 0; m < 4; ++m)
; #pragma unroll
;                 for (int n = 0; n < 2; ++n) acc[a][b][m][n] = (f32x4){0.f, 0.f, 0.f, 0.f};
;     bf16x8 At[4][2], B0[2][2], B1[2][2];
;     const char* cA = (const char*)g.A + (size_t)cur.pm * tstep; const char* cB = (const char*)g.Bt + (size_t)cur.pn * tstep;
;     S.a_ready(cur);
;     if constexpr (SP2) {
;         PG8_STAGE(PG8_SB(0, 0), cB, voffB); PG8_STAGE(PG8_SB(0, 1), cB + hstep, voffB); PG8_STAGE(PG8_SA(0, 0), cA, voffA); PG8_STAGE(PG8_SA(0, 1), cA + hstepA, voffA);
;         if (wr == 1) PG8_BAR;
;         PG8_WAIT_V(2); PG8_BAR;
;         PG8_STAGE(PG8_SB(1, 0), cB + kstep, voffB); PG8_STAGE(PG8_SA(1, 0), cA + kstepA, voffA); PG8_STAGE(PG8_SB(1, 1), cB + hstep + kstep, voffB);
;         PG8_WAIT_V(0); PG8_BAR;
;     } else {
.LBB0_490:
	s_andn2_b64 vcc, exec, s[4:5]
	v_readlane_b32 s4, v254, 25
	v_readlane_b32 s5, v254, 26
	s_nop 1
	v_cndmask_b32_e64 v1, 0, 1, s[4:5]
	v_cmp_ne_u32_e64 s[4:5], 1, v1
	s_nop 1
	v_writelane_b32 v252, s4, 25
	s_nop 1
	v_writelane_b32 v252, s5, 26
	s_cbranch_vccnz .LBB0_581
	v_readlane_b32 s6, v252, 25
	v_mov_b32_e32 v1, v0
	s_mov_b64 s[4:5], s[66:67]
	s_nop 0
	v_mov_b32_e32 v13, v0
	v_readlane_b32 s7, v252, 26
	s_and_b64 vcc, exec, s[6:7]
	v_readfirstlane_b32 s42, v13
	s_cbranch_vccnz .LBB0_531
	v_lshlrev_b32_e32 v1, 4, v13
	v_add_u32_e32 v2, 0x2000, v1
	v_ashrrev_i32_e32 v4, 31, v2
	v_lshrrev_b32_e32 v4, 22, v4
	v_add_u32_e32 v4, v2, v4
	v_ashrrev_i32_e32 v4, 10, v4
	s_waitcnt lgkmcnt(0)
	v_mul_i32_i24_e32 v5, 0x400, v4
	v_sub_u32_e32 v2, v2, v5
	v_lshrrev_b32_e32 v5, 4, v2
	v_bitop3_b32 v2, v5, v2, 32 bitop3:0x6c
	v_ashrrev_i32_e32 v5, 31, v2
	v_lshrrev_b32_e32 v5, 26, v5
	v_add_u32_e32 v5, v2, v5
	v_lshlrev_b32_e32 v7, 3, v4
	v_ashrrev_i32_e32 v6, 6, v5
	v_and_b32_e32 v7, -16, v7
	v_add_u32_e32 v8, v6, v7
	v_and_b32_e32 v6, 3, v6
	s_mov_b32 s18, 0x1ffffe0
	v_lshrrev_b32_e32 v7, 2, v8
	v_lshlrev_b32_e32 v9, 1, v8
	v_and_b32_e32 v5, 0xc0, v5
	v_and_or_b32 v6, v8, s18, v6
	v_and_b32_e32 v7, 4, v7
	v_and_b32_e32 v9, 24, v9
	v_lshlrev_b32_e32 v4, 5, v4
	v_sub_u32_e32 v2, v2, v5
	v_or3_b32 v6, v6, v7, v9
	s_movk_i32 s19, 0x580
	v_and_b32_e32 v4, 32, v4
	v_ashrrev_i16_sdwa v2, v244, sext(v2) dst_sel:DWORD dst_unused:UNUSED_PAD src0_sel:DWORD src1_sel:BYTE_0
	v_mul_lo_u32 v6, v6, s19
	v_add_u32_sdwa v2, v4, sext(v2) dst_sel:DWORD dst_unused:UNUSED_PAD src0_sel:DWORD src1_sel:WORD_0
	s_waitcnt vmcnt(0)
	v_add_lshl_u32 v164, v6, v2, 1
	v_lshrrev_b32_e32 v9, 4, v2
	v_lshlrev_b32_e32 v2, 5, v2
	v_and_b32_e32 v11, 0x100, v2
	v_lshlrev_b32_e32 v2, 4, v8
	v_and_b32_e32 v12, 0xf0, v2
	v_bfe_i32 v2, v13, 27, 1
	v_lshrrev_b32_e32 v2, 22, v2
	s_load_dwordx2 s[40:41], s[4:5], 0xd0
	v_add_u32_e32 v2, v1, v2
	v_and_b32_e32 v2, 0xfffffc00, v2
	v_lshlrev_b32_e32 v5, 5, v8
	v_sub_u32_e32 v1, v1, v2
	v_readlane_b32 s4, v252, 18
	v_and_b32_e32 v10, 0x600, v5
	v_lshrrev_b32_e32 v2, 4, v1
	v_ashrrev_i32_e32 v5, 31, v13
	s_mul_i32 s4, s4, 0x2d80000
	v_lshrrev_b32_e32 v4, 4, v8
	v_bitop3_b32 v1, v2, v1, 32 bitop3:0x6c
	v_lshrrev_b32_e32 v5, 26, v5
	v_readlane_b32 s5, v252, 19
	s_waitcnt lgkmcnt(0)
	s_add_u32 s4, s40, s4
	v_and_b32_e32 v4, 0xffffc, v4
	v_ashrrev_i32_e32 v2, 31, v1
	v_add_u32_e32 v5, v13, v5
	s_addc_u32 s5, s41, 0
	v_add_u32_e32 v4, v9, v4
	v_lshrrev_b32_e32 v2, 26, v2
	v_ashrrev_i32_e32 v5, 6, v5
	s_add_u32 s6, s40, 0xba00000
	v_lshl_or_b32 v4, v4, 12, v10
	v_add_u32_e32 v2, v1, v2
	v_lshlrev_b32_e32 v6, 3, v5
	s_addc_u32 s7, s41, 0
	v_or3_b32 v166, v4, v11, v12
	v_ashrrev_i32_e32 v4, 6, v2
	v_and_b32_e32 v6, -16, v6
	s_add_u32 s8, s4, 0x2900000
	v_add_u32_e32 v14, v4, v6
	s_addc_u32 s9, s5, 0
	s_ashr_i32 s5, s42, 6
	v_and_b32_e32 v4, 3, v4
	v_lshrrev_b32_e32 v6, 2, v14
	v_lshlrev_b32_e32 v7, 1, v14
	v_and_b32_e32 v2, 0xc0, v2
	s_ashr_i32 s4, s42, 8
	s_lshl_b32 s17, s5, 10
	v_and_or_b32 v4, v14, s18, v4
	v_and_b32_e32 v6, 4, v6
	v_and_b32_e32 v7, 24, v7
	v_lshlrev_b32_e32 v5, 5, v5
	v_sub_u32_e32 v1, v1, v2
	v_readlane_b32 s18, v254, 59
	v_or3_b32 v4, v4, v6, v7
	v_and_b32_e32 v5, 32, v5
	v_ashrrev_i16_sdwa v1, v244, sext(v1) dst_sel:DWORD dst_unused:UNUSED_PAD src0_sel:DWORD src1_sel:BYTE_0
	s_add_u32 s56, s8, s18
	v_readlane_b32 s18, v254, 57
	v_mul_lo_u32 v4, v4, s19
	v_add_u32_sdwa v1, v5, sext(v1) dst_sel:DWORD dst_unused:UNUSED_PAD src0_sel:DWORD src1_sel:WORD_0
	s_addc_u32 s57, s9, s18
	s_add_i32 s18, s17, 0
	v_add_lshl_u32 v2, v4, v1, 1
	s_add_i32 m0, s18, 0x10000
	v_lshrrev_b32_e32 v4, 4, v14
	global_load_lds_dwordx4 v2, s[56:57]
	s_add_i32 m0, s18, 0x12000
	s_add_u32 s20, s56, 0x58000
	v_lshrrev_b32_e32 v15, 4, v1
	v_and_b32_e32 v4, 0xffffc, v4
	v_lshlrev_b32_e32 v5, 5, v14
	v_lshlrev_b32_e32 v1, 5, v1
	global_load_lds_dwordx4 v164, s[56:57]
	s_addc_u32 s21, s57, 0
	s_add_i32 m0, s18, 0x14000
	v_add_u32_e32 v4, v15, v4
	v_and_b32_e32 v16, 0x600, v5
	v_and_b32_e32 v17, 0x100, v1
	v_lshlrev_b32_e32 v1, 4, v14
	global_load_lds_dwordx4 v2, s[20:21]
	s_add_i32 m0, s18, 0x16000
	v_readlane_b32 s19, v254, 56
	v_lshl_or_b32 v4, v4, 12, v16
	v_and_b32_e32 v18, 0xf0, v1
	s_add_u32 s54, s6, s19
	v_readlane_b32 s19, v254, 55
	v_or3_b32 v168, v4, v17, v18
	global_load_lds_dwordx4 v164, s[20:21]
	s_addc_u32 s55, s7, s19
	v_mov_b32_e32 v169, v3
	s_mov_b32 m0, s18
	s_add_i32 s19, s18, 0x2000
	v_lshl_add_u64 v[4:5], s[54:55], 0, v[168:169]
	global_load_lds_dwordx4 v168, s[54:55]
	v_mov_b32_e32 v167, v3
	s_mov_b32 m0, s19
	s_add_i32 s20, s18, 0x4000
	v_lshl_add_u64 v[6:7], s[54:55], 0, v[166:167]
	global_load_lds_dwordx4 v166, s[54:55]
	v_lshl_add_u64 v[4:5], v[4:5], 0, s[24:25]
	s_mov_b32 m0, s20
	s_add_i32 s21, s18, 0x6000
	global_load_lds_dwordx4 v[4:5], off
	v_lshl_add_u64 v[4:5], v[6:7], 0, s[24:25]
	s_mov_b32 m0, s21
	v_mov_b32_e32 v165, v3
	global_load_lds_dwordx4 v[4:5], off
	s_cmp_eq_u32 s4, 1
	v_lshl_add_u64 v[4:5], s[56:57], 0, v[2:3]
	s_cselect_b64 s[38:39], -1, 0
	s_cmp_lg_u32 s4, 1
	v_lshl_add_u64 v[6:7], s[56:57], 0, v[164:165]
	s_cbranch_scc1 .LBB0_494
	s_barrier

; #define PG8_WAIT_V(n) asm volatile("s_waitcnt vmcnt(" #n ")" ::: "memory")
; #define PG8_BAR __builtin_amdgcn_s_barrier()
; template <class Epi, class Sched, bool ALIGN_EPI = false, bool SP2 = false, bool FP8 = false, bool ABLK = false>
; __device__ __forceinline__ void gemm_phase(PG8_LAS unsigned char* lds, const Gemm g, const Sched& S, const Epi& E) {
;     ...
;     const int tid = tid_, wid = __builtin_amdgcn_readfirstlane(tid >> 6), lane = tid & 63, wr = wid >> 2, wc = wid & 3, fr = lane & 15, fq = lane >> 4;
;     const int K = g.K, nt = K / BK;
;     unsigned voffA[2], voffB[2];
; #pragma unroll
;     for (int i = 0; i < 2; ++i) { int R, C; stage_rc(tid * 16 + i * 8192, R, C); const int Rb = Epi::PERM ? ((R & ~31) + perm32(R & 31)) : R;
;         voffA[i] = ABLK ? (unsigned)(((((R >> 6) * 4 + (C >> 4)) * 8 + ((R >> 4) & 3)) * 64 + ((C >> 3) & 1) * 32 + (R & 15) * 2) * 8) : (unsigned)(R * K + C) * 2u; voffB[i] = (unsigned)(Rb * K + C) * 2u; }
;     const size_t kstep = (size_t)(BK * 2);
;     const size_t hstep = (size_t)HALF * K * 2;
;     const size_t kstepA = ABLK ? (size_t)32768 : kstep, hstepA = ABLK ? (size_t)2048 : hstep;
;     const size_t tstep = 2 * hstep;
;     const unsigned ldsw = (unsigned)wid * 1024u;
;     const int aoff = lds_byte(wr * 64 + fr, fq * 8), boff = lds_byte(wc * 32 + fr, fq * 8);
;     ...
;     Unit cur, nxt; int ui = 0;
;     if (!S.next(0, cur)) return;
;     f32x4 acc[2][2][4][2];
; #pragma unroll
;     for (int a = 0; a < 2; ++a)
; #pragma unroll
;         for (int b = 0; b < 2; ++b)
; #pragma unroll
;             for (int m = 0; m < 4; ++m)
; #pragma unroll
;                 for (int n = 0; n < 2; ++n) acc[a][b][m][n] = (f32x4){0.f, 0.f, 0.f, 0.f};
;     bf16x8 At[4][2], B0[2][2], B1[2][2];
;     const char* cA = (const char*)g.A + (size_t)cur.pm * tstep; const char* cB = (const char*)g.Bt + (size_t)cur.pn * tstep;
;     S.a_ready(cur);
;     if constexpr (SP2) {
;         PG8_STAGE(PG8_SB(0, 0), cB, voffB); PG8_STAGE(PG8_SB(0, 1), cB + hstep, voffB); PG8_STAGE(PG8_SA(0, 0), cA, voffA); PG8_STAGE(PG8_SA(0, 1), cA + hstepA, voffA);
;         if (wr == 1) PG8_BAR;
;         PG8_WAIT_V(2); PG8_BAR;
;         PG8_STAGE(PG8_SB(1, 0), cB + kstep, voffB); PG8_STAGE(PG8_SA(1, 0), cA + kstepA, voffA); PG8_STAGE(PG8_SB(1, 1), cB + hstep + kstep, voffB);
;         PG8_WAIT_V(0); PG8_BAR;
;     } else {
.LBB0_583:
	s_andn2_b64 vcc, exec, s[4:5]
	v_writelane_b32 v252, s89, 27
	s_cbranch_vccnz .LBB0_936
	v_mov_b32_e32 v1, v0
	s_mov_b64 s[4:5], s[66:67]
	s_nop 0
	v_mov_b32_e32 v18, v0
	s_cmp_ge_i32 s2, s46
	s_nop 0
	v_readfirstlane_b32 s21, v18
	s_cbranch_scc1 .LBB0_886
	v_lshlrev_b32_e32 v1, 4, v18
	v_add_u32_e32 v2, 0x2000, v1
	v_ashrrev_i32_e32 v4, 31, v2
	v_lshrrev_b32_e32 v4, 22, v4
	v_add_u32_e32 v4, v2, v4
	v_ashrrev_i32_e32 v12, 10, v4
	v_mul_i32_i24_e32 v4, 0x400, v12
	v_sub_u32_e32 v2, v2, v4
	s_load_dwordx2 s[38:39], s[4:5], 0xd0
	v_readlane_b32 s4, v252, 18
	v_lshrrev_b32_e32 v4, 4, v2
	s_mul_i32 s4, s4, 0x2d80000
	v_bitop3_b32 v2, v4, v2, 32 bitop3:0x6c
	v_readlane_b32 s5, v252, 19
	s_add_i32 s4, s4, 0x2e80000
	v_ashrrev_i32_e32 v4, 31, v2
	s_lshr_b32 s6, s4, 19
	v_readlane_b32 s4, v254, 27
	s_ashr_i32 s5, s21, 6
	v_readlane_b32 s8, v254, 40
	v_lshrrev_b32_e32 v4, 26, v4
	s_add_i32 s17, s6, s4
	s_ashr_i32 s4, s21, 8
	s_lshl_b32 s7, s5, 10
	v_readlane_b32 s9, v254, 41
	v_add_u32_e32 v4, v2, v4
	s_waitcnt lgkmcnt(0)
	v_lshlrev_b32_e32 v5, 3, v12
	s_and_b64 s[8:9], s[8:9], exec
	v_ashrrev_i32_e32 v13, 6, v4
	v_and_b32_e32 v5, -16, v5
	v_readlane_b32 s8, v254, 39
	v_add_u32_e32 v5, v13, v5
	s_cselect_b32 s72, s17, s8
	v_and_b32_e32 v6, 3, v13
	s_mov_b32 s8, 0x1fffe0
	v_lshrrev_b32_e32 v7, 2, v5
	v_lshlrev_b32_e32 v8, 1, v5
	v_and_b32_e32 v4, 0xc0, v4
	v_and_or_b32 v6, v5, s8, v6
	v_and_b32_e32 v7, 4, v7
	v_and_b32_e32 v8, 24, v8
	v_sub_u32_e32 v2, v2, v4
	v_or3_b32 v6, v6, v7, v8
	v_lshlrev_b32_e32 v7, 5, v12
	v_ashrrev_i16_sdwa v2, v244, sext(v2) dst_sel:DWORD dst_unused:UNUSED_PAD src0_sel:DWORD src1_sel:BYTE_0
	v_and_b32_e32 v7, 32, v7
	v_bfe_i32 v14, v2, 0, 16
	v_add_lshl_u32 v2, v7, v14, 1
	s_waitcnt vmcnt(0)
	v_lshl_add_u32 v172, v6, 11, v2
	v_lshl_add_u32 v174, v5, 11, v2
	v_bfe_i32 v2, v18, 27, 1
	v_lshrrev_b32_e32 v2, 22, v2
	v_add_u32_e32 v2, v1, v2
	v_and_b32_e32 v2, 0xfffffc00, v2
	v_sub_u32_e32 v1, v1, v2
	v_lshrrev_b32_e32 v2, 4, v1
	v_ashrrev_i32_e32 v4, 31, v18
	v_bitop3_b32 v1, v2, v1, 32 bitop3:0x6c
	v_lshrrev_b32_e32 v4, 26, v4
	v_ashrrev_i32_e32 v2, 31, v1
	v_add_u32_e32 v4, v18, v4
	v_lshrrev_b32_e32 v2, 26, v2
	v_ashrrev_i32_e32 v16, 6, v4
	v_add_u32_e32 v2, v1, v2
	v_lshlrev_b32_e32 v4, 3, v16
	v_ashrrev_i32_e32 v15, 6, v2
	v_and_b32_e32 v4, -16, v4
	v_add_u32_e32 v4, v15, v4
	v_and_b32_e32 v5, 3, v15
	v_lshrrev_b32_e32 v6, 2, v4
	v_lshlrev_b32_e32 v7, 1, v4
	v_and_b32_e32 v2, 0xc0, v2
	v_and_or_b32 v5, v4, s8, v5
	v_and_b32_e32 v6, 4, v6
	v_and_b32_e32 v7, 24, v7
	v_sub_u32_e32 v1, v1, v2
	s_ashr_i32 s73, s72, 31
	v_or3_b32 v5, v5, v6, v7
	v_lshlrev_b32_e32 v6, 5, v16
	v_ashrrev_i16_sdwa v1, v244, sext(v1) dst_sel:DWORD dst_unused:UNUSED_PAD src0_sel:DWORD src1_sel:BYTE_0
	s_lshl_b64 s[8:9], s[72:73], 19
	v_and_b32_e32 v6, 32, v6
	v_bfe_i32 v17, v1, 0, 16
	s_add_u32 s44, s38, s8
	v_add_lshl_u32 v1, v6, v17, 1
	s_addc_u32 s45, s39, s9
	s_add_i32 s8, s7, 0
	v_lshl_add_u32 v2, v5, 11, v1
	s_add_i32 m0, s8, 0x10000
	v_lshl_add_u32 v176, v4, 11, v1
	global_load_lds_dwordx4 v2, s[44:45]
	s_add_i32 m0, s8, 0x12000
	s_add_u32 s18, s44, 0x40000
	global_load_lds_dwordx4 v172, s[44:45]
	s_addc_u32 s19, s45, 0
	s_add_i32 m0, s8, 0x14000
	v_mov_b32_e32 v173, v3
	global_load_lds_dwordx4 v2, s[18:19]
	s_add_i32 m0, s8, 0x16000
	v_mov_b32_e32 v177, v3
	global_load_lds_dwordx4 v172, s[18:19]
	v_readlane_b32 s18, v254, 44
	v_readlane_b32 s19, v254, 45
	s_add_u32 s42, s38, s18
	s_addc_u32 s43, s39, s19
	s_add_i32 s9, s8, 0x2000
	s_mov_b32 m0, s8
	s_add_u32 s22, s42, 0x40000
	global_load_lds_dwordx4 v176, s[42:43]
	s_mov_b32 m0, s9
	s_addc_u32 s23, s43, 0
	s_add_i32 s17, s8, 0x4000
	global_load_lds_dwordx4 v174, s[42:43]
	s_mov_b32 m0, s17
	s_add_i32 s18, s8, 0x6000
	global_load_lds_dwordx4 v176, s[22:23]
	s_mov_b32 m0, s18
	v_mov_b32_e32 v175, v3
	global_load_lds_dwordx4 v174, s[22:23]
	s_cmp_eq_u32 s4, 1
	v_lshl_add_u64 v[10:11], s[44:45], 0, v[2:3]
	v_lshl_add_u64 v[8:9], s[44:45], 0, v[172:173]
	v_lshl_add_u64 v[4:5], s[42:43], 0, v[176:177]
	s_cselect_b64 s[48:49], -1, 0
	s_cmp_lg_u32 s4, 1
	v_lshl_add_u64 v[6:7], s[42:43], 0, v[174:175]
	s_cbranch_scc1 .LBB0_587
	s_barrier

; #define GAS __attribute__((address_space(1)))
; #define LAS __attribute__((address_space(3)))
; #define REP(n) for (int rep_ = 0; rep_ < 1 + MK_REPN * (((MK_DUP) >> (n)) & 1); ++rep_)
; #define PHASE_BEGIN() do { int t_ = threadIdx.x; asm volatile("" : "+v"(t_)); F.tid = t_; F.lane = t_ & 63; F.wave = __builtin_amdgcn_readfirstlane(t_ >> 6); \
;         A = (KArgs)__builtin_amdgcn_kernarg_segment_ptr(); asm volatile("" : "+s"(A)); ws = A->ws; F.ws = ws; F.ctl = (gu32*)(ws + WS_CTL); } while (0)
; __device__ __forceinline__ void conv_a_unit(Frame& F, const bf16* HG, bf16* MIX, const float* dw, const float* dwb, const float* lng, const float* lnb, int unit) {
;     const int tid = F.tid, lane = F.lane, wave = F.wave;
;     const int row0 = unit * 64, t0 = row0 % SEQ;
;     LAS unsigned short* hb = (LAS unsigned short*)(F.lds + RING_OFF); LAS float* yb = (LAS float*)(F.lds + RING_OFF + 49152);
;     for (int ch = tid; ch < 94 * 32; ch += NWAVES * 64) { const int rr = ch >> 5, c16 = ch & 31; const int t = t0 - 30 + rr;
;         v4u v = (v4u){0u, 0u, 0u, 0u}; if (t >= 0) v = *(const GAS v4u*)(HG + (size_t)(row0 - 30 + rr) * 256 + c16 * 8);
;         *(LAS v4u*)(hb + rr * 256 + c16 * 8) = v; }
;     __syncthreads();
;     { const int c = tid & 255, half = tid >> 8;
;       float w[31];
; #pragma unroll
;       for (int j = 0; j < 31; ++j) w[j] = dw[j * 256 + c];
;       const float bias = dwb[c];
; __global__ void __launch_bounds__(NWAVES * 64, 2) mk_fwd(Args args) {
;     ...
;         if (EN(5) && IN(pb + 3)) { PHASE_BEGIN(); REP(5) {
;             REP(10) for (int u = F.vcu; u < M / 64; u += F.G) conv_a_unit(F, (const bf16*)(ws + WS_HG), (bf16*)(ws + WS_MIX), INF(A, I_CONF_DW) + l * 31 * 256, INF(A, I_CONF_DW_B) + l * 256, INF(A, I_CONF_LN_G) + l * 256, INF(A, I_CONF_LN_B) + l * 256, u);
.LBB0_938:
	s_andn2_b64 vcc, exec, s[4:5]
	s_cbranch_vccnz .LBB0_1256
	v_mov_b32_e32 v1, v0
	v_readlane_b32 s6, v254, 28
	v_readfirstlane_b32 s4, v1
	s_ashr_i32 s38, s4, 6
	s_mov_b64 s[4:5], s[66:67]
	s_nop 0
	s_load_dwordx2 s[44:45], s[4:5], 0xd0
	s_load_dwordx2 s[46:47], s[4:5], 0x68
	v_and_b32_e32 v226, 63, v1
	v_readlane_b32 s7, v254, 29
	v_and_b32_e32 v194, 31, v1
	v_lshlrev_b32_e32 v32, 4, v226
	s_and_b64 vcc, exec, s[6:7]
	s_cbranch_vccz .LBB0_950
	s_load_dwordx8 s[52:59], s[4:5], 0x48
	v_readlane_b32 s4, v252, 18
	s_cmp_lt_i32 s38, 64
	v_readlane_b32 s5, v252, 19
	v_lshlrev_b32_e32 v2, 4, v194
	s_cselect_b64 s[48:49], -1, 0
	s_lshl_b32 s92, s4, 8
	s_mulk_i32 s4, 0x1f00
	s_mov_b32 s5, s93
	s_waitcnt lgkmcnt(0)
	v_lshl_add_u64 v[4:5], s[44:45], 0, v[2:3]
	s_mov_b64 s[20:21], 0xba00000
	v_add_u32_e32 v82, 0, v2
	v_ashrrev_i32_e32 v2, 8, v1
	s_lshl_b64 s[4:5], s[4:5], 2
	v_lshl_add_u64 v[12:13], v[4:5], 0, s[20:21]
	v_lshlrev_b32_e32 v4, 14, v2
	v_lshlrev_b32_sdwa v5, v244, v1 dst_sel:DWORD dst_unused:UNUSED_PAD src0_sel:DWORD src1_sel:BYTE_0
	s_add_u32 s4, s52, s4
	v_add3_u32 v83, 0, v4, v5
	v_mov_b32_e32 v4, 2
	s_addc_u32 s5, s53, s5
	v_lshlrev_b32_sdwa v4, v4, v1 dst_sel:DWORD dst_unused:UNUSED_PAD src0_sel:DWORD src1_sel:BYTE_0
	v_mov_b32_e32 v5, v3
	v_lshl_add_u64 v[16:17], s[4:5], 0, v[4:5]
	s_mov_b64 s[4:5], 0x1000
	v_lshl_add_u64 v[18:19], v[16:17], 0, s[4:5]
	s_mov_b64 s[4:5], 0x1400
	v_lshl_add_u64 v[20:21], v[16:17], 0, s[4:5]
	s_mov_b64 s[4:5], 0x1800
	v_lshl_add_u64 v[22:23], v[16:17], 0, s[4:5]
	s_mov_b64 s[4:5], 0x1c00
	v_lshl_add_u64 v[24:25], v[16:17], 0, s[4:5]
	s_mov_b64 s[4:5], 0x2000
	v_lshl_add_u64 v[26:27], v[16:17], 0, s[4:5]
	s_mov_b64 s[4:5], 0x2400
	v_lshl_add_u64 v[28:29], v[16:17], 0, s[4:5]
	s_mov_b64 s[4:5], 0x2800
	v_lshl_add_u64 v[30:31], v[16:17], 0, s[4:5]
	s_mov_b64 s[4:5], 0x2c00
	v_lshl_add_u64 v[34:35], v[16:17], 0, s[4:5]
	s_mov_b64 s[4:5], 0x3000
	v_lshl_add_u64 v[36:37], v[16:17], 0, s[4:5]
	s_mov_b64 s[4:5], 0x3400
	v_lshl_add_u64 v[38:39], v[16:17], 0, s[4:5]
	s_mov_b64 s[4:5], 0x3800
	v_lshl_add_u64 v[40:41], v[16:17], 0, s[4:5]
	s_mov_b64 s[4:5], 0x3c00
	v_lshl_add_u64 v[42:43], v[16:17], 0, s[4:5]
	s_mov_b64 s[4:5], 0x4000
	v_lshl_add_u64 v[44:45], v[16:17], 0, s[4:5]
	s_mov_b64 s[4:5], 0x4400
	v_lshl_add_u64 v[46:47], v[16:17], 0, s[4:5]
	s_mov_b64 s[4:5], 0x4800
	v_lshl_add_u64 v[48:49], v[16:17], 0, s[4:5]
	s_mov_b64 s[4:5], 0x4c00
	v_lshl_add_u64 v[50:51], v[16:17], 0, s[4:5]
	s_mov_b64 s[4:5], 0x5000
	v_lshl_add_u64 v[52:53], v[16:17], 0, s[4:5]
	s_mov_b64 s[4:5], 0x5400
	v_lshl_add_u64 v[54:55], v[16:17], 0, s[4:5]
	s_mov_b64 s[4:5], 0x5800
	v_lshl_add_u64 v[56:57], v[16:17], 0, s[4:5]
	s_mov_b64 s[4:5], 0x5c00
	v_lshl_add_u64 v[58:59], v[16:17], 0, s[4:5]
	s_mov_b64 s[4:5], 0x6000
	s_lshl_b64 s[6:7], s[92:93], 2
	v_lshl_add_u64 v[60:61], v[16:17], 0, s[4:5]
	s_mov_b64 s[4:5], 0x6400
	s_add_u32 s8, s54, s6
	v_lshl_add_u64 v[62:63], v[16:17], 0, s[4:5]
	s_mov_b64 s[4:5], 0x6800
	s_addc_u32 s9, s55, s7
	v_lshl_add_u64 v[64:65], v[16:17], 0, s[4:5]
	s_mov_b64 s[4:5], 0x6c00
	s_add_u32 s18, s56, s6
	v_lshl_add_u64 v[66:67], v[16:17], 0, s[4:5]
	s_mov_b64 s[4:5], 0x7000
	s_addc_u32 s19, s57, s7
	s_waitcnt vmcnt(0)
	v_lshl_add_u64 v[68:69], v[16:17], 0, s[4:5]
	s_mov_b64 s[4:5], 0x7400
	s_add_u32 s6, s58, s6
	v_lshl_add_u64 v[70:71], v[16:17], 0, s[4:5]
	s_mov_b64 s[4:5], 0x7800
	s_addc_u32 s7, s59, s7
	v_lshlrev_b32_e32 v2, 15, v2
	v_lshl_add_u64 v[72:73], v[16:17], 0, s[4:5]
	s_lshl_b32 s4, s38, 10
	v_add3_u32 v84, 0, v2, v4
	v_lshlrev_b32_e32 v2, 3, v226
	s_add_i32 s4, s4, 0
	s_movk_i32 s17, 0xbc0
	v_lshl_add_u64 v[6:7], s[44:45], 0, v[2:3]
	s_mov_b64 s[20:21], 0x15f00000
	v_mov_b32_e32 v33, v3
	s_add_i32 s4, s4, 0xc000
	v_cmp_gt_i32_e64 s[40:41], s17, v1
	v_add_u32_e32 v85, 0xc000, v84
	v_lshl_add_u64 v[14:15], v[6:7], 0, s[20:21]
	v_lshl_add_u64 v[74:75], s[8:9], 0, v[4:5]
	v_lshl_add_u64 v[76:77], s[18:19], 0, v[32:33]
	v_lshl_add_u64 v[78:79], s[6:7], 0, v[32:33]
	v_add_u32_e32 v2, s4, v32
	v_readlane_b32 s17, v254, 60
	v_readlane_b32 s18, v253, 2
	s_branch .LBB0_942
